# speedup vs baseline: 1.0096x; 1.0096x over previous
.LBB2_11:
	s_or_b64 exec, exec, s[8:9]
	v_or_b32_e32 v1, 31, v1
	v_min_i32_e32 v2, 0x247, v1
	v_add_u32_e32 v2, 64, v2
	v_ashrrev_i32_e32 v2, 6, v2
	v_cmp_lt_i32_e32 vcc, s18, v1
	v_mov_b32_e32 v17, 0
	v_mov_b32_e32 v35, 0
	v_cndmask_b32_e32 v85, 9, v2, vcc
	v_readfirstlane_b32 s28, v97
	s_cmp_lt_u32 s28, 16
	s_cselect_b32 s29, 1, 0
	s_cmp_eq_u32 s28, 18
	s_cselect_b32 s28, 1, 0
	s_or_b32 s29, s29, s28
	v_subrev_u32_e32 v85, s29, v85
	v_cmp_lt_i32_e32 vcc, 0, v85
	v_mov_b32_e32 v34, 0
	v_mov_b32_e32 v14, 0
	v_mov_b32_e32 v13, 0
	v_mov_b32_e32 v37, 0
	v_mov_b32_e32 v36, 0
	v_mov_b32_e32 v10, 0
	v_mov_b32_e32 v9, 0
	v_mov_b32_e32 v39, 0
	v_mov_b32_e32 v38, 0
	v_mov_b32_e32 v6, 0
	v_mov_b32_e32 v5, 0
	v_mov_b32_e32 v41, 0
	v_mov_b32_e32 v40, 0
	v_mov_b32_e32 v2, 0
	v_mov_b32_e32 v33, 0
	v_mov_b32_e32 v43, 0
	v_mov_b32_e32 v42, 0
	v_mov_b32_e32 v30, 0
	v_mov_b32_e32 v29, 0
	v_mov_b32_e32 v45, 0
	v_mov_b32_e32 v44, 0
	v_mov_b32_e32 v26, 0
	v_mov_b32_e32 v25, 0
	v_mov_b32_e32 v47, 0
	v_mov_b32_e32 v46, 0
	v_mov_b32_e32 v22, 0
	v_mov_b32_e32 v21, 0
	v_mov_b32_e32 v49, 0
	v_mov_b32_e32 v48, 0
	v_mov_b32_e32 v18, 0
	v_mov_b32_e32 v1, 0
	s_and_saveexec_b64 s[8:9], vcc
	s_cbranch_execz .LBB2_23
	v_mov_b32_e32 v14, v0
	v_mov_b32_e32 v15, v0
	v_max_i32_e32 v98, 0x205, v3
	v_mov_b32_e32 v1, v0
	v_mov_b32_e32 v2, v0
	v_mov_b32_e32 v3, v0
	v_mov_b32_e32 v4, v0
	v_mov_b32_e32 v5, v0
	v_mov_b32_e32 v6, v0
	v_mov_b32_e32 v7, v0
	v_mov_b32_e32 v8, v0
	v_mov_b32_e32 v9, v0
	v_mov_b32_e32 v10, v0
	v_mov_b32_e32 v11, v0
	v_mov_b32_e32 v12, v0
	v_mov_b32_e32 v13, v0
	v_mov_b64_e32 v[32:33], v[14:15]
	v_mov_b64_e32 v[30:31], v[12:13]
	v_mov_b64_e32 v[28:29], v[10:11]
	v_mov_b64_e32 v[26:27], v[8:9]
	v_mov_b64_e32 v[24:25], v[6:7]
	v_mov_b64_e32 v[22:23], v[4:5]
	v_mov_b64_e32 v[20:21], v[2:3]
	v_mov_b64_e32 v[18:19], v[0:1]
	v_mov_b64_e32 v[16:17], v[14:15]
	s_mov_b32 s21, 0
	v_mov_b32_e32 v104, 0
	s_mov_b32 s31, 0
	s_mov_b64 s[10:11], 0
	v_mov_b64_e32 v[14:15], v[12:13]
	v_mov_b64_e32 v[12:13], v[10:11]
	v_mov_b64_e32 v[10:11], v[8:9]
	v_mov_b64_e32 v[8:9], v[6:7]
	v_mov_b64_e32 v[6:7], v[4:5]
	v_mov_b64_e32 v[4:5], v[2:3]
	v_mov_b64_e32 v[2:3], v[0:1]
	v_mov_b32_e32 v1, 0
	v_mov_b32_e32 v99, v88
	v_mov_b32_e32 v100, v89
	v_mov_b32_e32 v101, v90
	v_mov_b32_e32 v102, v91
	v_mov_b32_e32 v103, v93
	v_readfirstlane_b32 s30, v85
	v_mov_b32_e32 v117, v114
	v_mov_b32_e32 v118, v115
	v_mov_b32_e32 v119, v116
	s_branch .LBB2_14
.LBB2_13:
	v_exp_f32_e32 v105, v50
	v_exp_f32_e32 v106, v51
	v_exp_f32_e32 v107, v52
	v_exp_f32_e32 v108, v53
	ds_read_b128 v[50:53], v103
	v_exp_f32_e32 v109, v54
	v_exp_f32_e32 v110, v55
	v_exp_f32_e32 v111, v56
	v_exp_f32_e32 v57, v57
	v_cvt_pkrtz_f16_f32 v54, v105, v106
	v_cvt_pkrtz_f16_f32 v55, v107, v108
	v_cvt_pkrtz_f16_f32 v56, v109, v110
	v_cvt_pkrtz_f16_f32 v57, v111, v57
	ds_read_b128 v[106:109], v117
	v_exp_f32_e32 v105, v58
	s_waitcnt lgkmcnt(1)
	v_mfma_f32_32x32x16_f16 v[18:33], v[50:53], v[54:57], v[18:33]
	ds_read_b128 v[50:53], v103 offset:4096
	v_exp_f32_e32 v110, v59
	v_exp_f32_e32 v111, v60
	v_exp_f32_e32 v112, v61
	ds_read_b128 v[58:61], v117 offset:4096
	v_exp_f32_e32 v62, v62
	v_exp_f32_e32 v41, v41
	s_waitcnt lgkmcnt(1)
	v_mfma_f32_32x32x16_f16 v[2:17], v[50:53], v[54:57], v[2:17]
	v_exp_f32_e32 v52, v63
	v_exp_f32_e32 v53, v64
	v_exp_f32_e32 v63, v65
	v_cvt_pkrtz_f16_f32 v50, v105, v110
	v_cvt_pkrtz_f16_f32 v51, v111, v112
	v_cvt_pkrtz_f16_f32 v52, v62, v52
	v_cvt_pkrtz_f16_f32 v53, v53, v63
	v_exp_f32_e32 v62, v34
	v_exp_f32_e32 v63, v35
	v_exp_f32_e32 v64, v36
	v_exp_f32_e32 v65, v37
	ds_read_b128 v[34:37], v118
	v_mfma_f32_32x32x16_f16 v[18:33], v[106:109], v[50:53], v[18:33]
	v_exp_f32_e32 v105, v38
	v_exp_f32_e32 v106, v39
	v_cvt_pkrtz_f16_f32 v38, v62, v63
	v_cvt_pkrtz_f16_f32 v39, v64, v65
	v_exp_f32_e32 v62, v42
	v_exp_f32_e32 v63, v43
	v_exp_f32_e32 v64, v44
	s_waitcnt lgkmcnt(1)
	v_mfma_f32_32x32x16_f16 v[2:17], v[58:61], v[50:53], v[2:17]
	v_exp_f32_e32 v58, v40
	v_cvt_pkrtz_f16_f32 v40, v105, v106
	v_exp_f32_e32 v65, v45
	ds_read_b128 v[42:45], v119 offset:4096
	v_cvt_pkrtz_f16_f32 v41, v58, v41
	ds_read_b128 v[58:61], v119
	v_exp_f32_e32 v46, v46
	s_waitcnt lgkmcnt(2)
	v_mfma_f32_32x32x16_f16 v[18:33], v[34:37], v[38:41], v[18:33]
	ds_read_b128 v[34:37], v118 offset:4096
	s_add_i32 s21, s21, 64
	v_add_u32_e32 v99, 0x2000, v99
	v_add_u32_e32 v100, 0x2000, v100
	v_add_u32_e32 v101, 0x2000, v101
	s_waitcnt lgkmcnt(0)
	v_mfma_f32_32x32x16_f16 v[2:17], v[34:37], v[38:41], v[2:17]
	v_exp_f32_e32 v36, v47
	v_exp_f32_e32 v37, v48
	v_exp_f32_e32 v47, v49
	v_cvt_pkrtz_f16_f32 v34, v62, v63
	v_cvt_pkrtz_f16_f32 v35, v64, v65
	v_cvt_pkrtz_f16_f32 v36, v46, v36
	v_cvt_pkrtz_f16_f32 v37, v37, v47
	v_pk_add_f16 v46, v55, v51
	v_pk_add_f16 v47, v57, v53
	v_pk_add_f16 v48, v54, v50
	v_pk_add_f16 v49, v56, v52
	v_pk_add_f16 v39, v39, v35
	v_pk_add_f16 v41, v41, v37
	v_pk_add_f16 v38, v38, v34
	v_pk_add_f16 v40, v40, v36
	v_pk_add_f16 v38, v38, v48
	v_pk_add_f16 v40, v40, v49
	v_pk_add_f16 v41, v41, v47
	v_pk_add_f16 v39, v39, v46
	v_mfma_f32_32x32x16_f16 v[18:33], v[58:61], v[34:37], v[18:33]
	v_pk_add_f16 v39, v39, v41
	v_pk_add_f16 v38, v38, v40
	v_add_u32_e32 v102, 0x2000, v102
	v_mfma_f32_32x32x16_f16 v[2:17], v[42:45], v[34:37], v[2:17]
	v_fma_mix_f32 v1, v39, 1.0, v1 op_sel_hi:[1,0,0]
	v_fma_mix_f32 v1, v39, 1.0, v1 op_sel:[1,0,0] op_sel_hi:[1,0,0]
	v_fma_mix_f32 v1, v38, 1.0, v1 op_sel_hi:[1,0,0]
	v_fma_mix_f32 v1, v38, 1.0, v1 op_sel:[1,0,0] op_sel_hi:[1,0,0]
	s_add_i32 s30, s30, -1
	v_add_u32_e32 v103, 0x2000, v103
	v_add_u32_e32 v117, 0x2000, v117
	v_add_u32_e32 v118, 0x2000, v118
	v_add_u32_e32 v119, 0x2000, v119
	s_cmp_eq_u32 s30, 0
	s_cbranch_scc1 .LBB2_22

.LBB2_16:
	s_nop 9
	v_max_f32_e32 v105, v50, v51
	v_max3_f32 v106, v34, v35, v36
	v_max3_f32 v105, v105, v52, v53
	v_max3_f32 v105, v105, v37, v54
	v_max3_f32 v106, v106, v38, v39
	v_max3_f32 v105, v105, v55, v56
	v_max3_f32 v106, v106, v40, v41
	v_max3_f32 v105, v105, v57, v58
	v_max3_f32 v106, v106, v42, v43
	v_max3_f32 v105, v105, v59, v60
	v_max3_f32 v106, v106, v44, v45
	v_max3_f32 v105, v105, v61, v62
	v_max3_f32 v106, v106, v46, v47
	v_max3_f32 v105, v105, v63, v64
	v_max3_f32 v106, v106, v48, v49
	v_max3_f32 v105, v105, v65, v106
	v_mov_b32_e32 v106, v105
	s_nop 1
	v_permlane32_swap_b32_e32 v105, v106
	v_max_f32_e32 v105, v105, v106
	v_sub_f32_e32 v106, v105, v104
	v_cmp_lt_f32_e32 vcc, s19, v106
	s_cmp_lg_u32 s21, 0
	s_cbranch_scc1 .Lat_thr
	v_cmp_gt_f32_e64 s[16:17], s20, v105
	s_or_b64 vcc, vcc, s[16:17]
.Lat_thr:
	s_mov_b64 s[14:15], vcc
	s_cbranch_vccz .LBB2_20
	v_cndmask_b32_e64 v105, v104, v105, s[14:15]
	v_sub_f32_e32 v104, v104, v105
	v_exp_f32_e32 v104, v104
	s_nop 0
	v_pk_mul_f32 v[32:33], v[104:105], v[32:33] op_sel_hi:[0,1]
	v_pk_mul_f32 v[30:31], v[104:105], v[30:31] op_sel_hi:[0,1]
	v_pk_mul_f32 v[28:29], v[104:105], v[28:29] op_sel_hi:[0,1]
	v_pk_mul_f32 v[26:27], v[104:105], v[26:27] op_sel_hi:[0,1]
	v_pk_mul_f32 v[24:25], v[104:105], v[24:25] op_sel_hi:[0,1]
	v_pk_mul_f32 v[22:23], v[104:105], v[22:23] op_sel_hi:[0,1]
	v_pk_mul_f32 v[20:21], v[104:105], v[20:21] op_sel_hi:[0,1]
	v_pk_mul_f32 v[18:19], v[104:105], v[18:19] op_sel_hi:[0,1]
	v_pk_mul_f32 v[16:17], v[104:105], v[16:17] op_sel_hi:[0,1]
	v_pk_mul_f32 v[14:15], v[104:105], v[14:15] op_sel_hi:[0,1]
	v_pk_mul_f32 v[12:13], v[104:105], v[12:13] op_sel_hi:[0,1]
	v_pk_mul_f32 v[10:11], v[104:105], v[10:11] op_sel_hi:[0,1]
	v_pk_mul_f32 v[8:9], v[104:105], v[8:9] op_sel_hi:[0,1]
	v_pk_mul_f32 v[6:7], v[104:105], v[6:7] op_sel_hi:[0,1]
	v_pk_mul_f32 v[4:5], v[104:105], v[4:5] op_sel_hi:[0,1]
	v_pk_mul_f32 v[2:3], v[104:105], v[2:3] op_sel_hi:[0,1]
	v_mul_f32_e32 v1, v1, v104
	v_mov_b32_e32 v104, v105
	s_mov_b32 s31, 1
.LBB2_20:
	s_cmp_eq_u32 s31, 0
	s_cbranch_scc1 .LBB2_13
	v_sub_f32_e32 v50, v50, v104
	v_sub_f32_e32 v51, v51, v104
	v_sub_f32_e32 v52, v52, v104
	v_sub_f32_e32 v53, v53, v104
	v_sub_f32_e32 v54, v54, v104
	v_sub_f32_e32 v55, v55, v104
	v_sub_f32_e32 v56, v56, v104
	v_sub_f32_e32 v57, v57, v104
	v_sub_f32_e32 v58, v58, v104
	v_sub_f32_e32 v59, v59, v104
	v_sub_f32_e32 v60, v60, v104
	v_sub_f32_e32 v61, v61, v104
	v_sub_f32_e32 v62, v62, v104
	v_sub_f32_e32 v63, v63, v104
	v_sub_f32_e32 v64, v64, v104
	v_sub_f32_e32 v65, v65, v104
	v_sub_f32_e32 v34, v34, v104
	v_sub_f32_e32 v35, v35, v104
	v_sub_f32_e32 v36, v36, v104
	v_sub_f32_e32 v37, v37, v104
	v_sub_f32_e32 v38, v38, v104
	v_sub_f32_e32 v39, v39, v104
	v_sub_f32_e32 v40, v40, v104
	v_sub_f32_e32 v41, v41, v104
	v_sub_f32_e32 v42, v42, v104
	v_sub_f32_e32 v43, v43, v104
	v_sub_f32_e32 v44, v44, v104
	v_sub_f32_e32 v45, v45, v104
	v_sub_f32_e32 v46, v46, v104
	v_sub_f32_e32 v47, v47, v104
	v_sub_f32_e32 v48, v48, v104
	v_sub_f32_e32 v49, v49, v104
	s_branch .LBB2_13
.LBB2_22:
	s_or_b64 exec, exec, s[10:11]
	s_cmp_lg_u32 s29, 0
	s_cbranch_scc1 .Lat_sp
.Lat_exit:
	s_nop 2
	v_mov_b32_e32 v35, v16
	v_mov_b32_e32 v34, v15
	v_mov_b32_e32 v37, v12
	v_mov_b32_e32 v36, v11
	v_mov_b32_e32 v39, v8
	v_mov_b32_e32 v38, v7
	v_mov_b32_e32 v41, v4
	v_mov_b32_e32 v40, v3
	v_mov_b32_e32 v43, v32
	v_mov_b32_e32 v42, v31
	v_mov_b32_e32 v45, v28
	v_mov_b32_e32 v44, v27
	v_mov_b32_e32 v47, v24
	v_mov_b32_e32 v46, v23
	v_mov_b32_e32 v49, v20
	v_mov_b32_e32 v48, v19

.Lat_sp:
	ds_read_b128 v[34:37], v99
	ds_read_b128 v[38:41], v100
	ds_read_b128 v[42:45], v101
	ds_read_b128 v[46:49], v102
	v_add_u32_e32 v113, s21, v92
	s_waitcnt lgkmcnt(3)
	v_mfma_f32_32x32x16_f16 v[50:65], v[34:37], v[66:69], 0
	s_waitcnt lgkmcnt(2)
	v_mfma_f32_32x32x16_f16 v[50:65], v[38:41], v[70:73], v[50:65]
	s_waitcnt lgkmcnt(1)
	v_mfma_f32_32x32x16_f16 v[50:65], v[42:45], v[74:77], v[50:65]
	s_waitcnt lgkmcnt(0)
	v_mfma_f32_32x32x16_f16 v[50:65], v[46:49], v[78:81], v[50:65]
	ds_read_b128 v[34:37], v103
	ds_read_b128 v[38:41], v103 offset:4096
	s_nop 7
	s_nop 3
	v_cmp_le_u32_e32 vcc, v113, v98
	v_add_u32_e32 v105, 1, v113
	s_nop 0
	v_cndmask_b32_e32 v50, v96, v50, vcc
	v_cmp_le_u32_e32 vcc, v105, v98
	v_add_u32_e32 v105, 2, v113
	s_nop 0
	v_cndmask_b32_e32 v51, v96, v51, vcc
	v_cmp_le_u32_e32 vcc, v105, v98
	v_add_u32_e32 v105, 3, v113
	s_nop 0
	v_cndmask_b32_e32 v52, v96, v52, vcc
	v_cmp_le_u32_e32 vcc, v105, v98
	v_add_u32_e32 v105, 4, v113
	s_nop 0
	v_cndmask_b32_e32 v53, v96, v53, vcc
	v_cmp_le_u32_e32 vcc, v105, v98
	v_add_u32_e32 v105, 5, v113
	s_nop 0
	v_cndmask_b32_e32 v54, v96, v54, vcc
	v_cmp_le_u32_e32 vcc, v105, v98
	v_add_u32_e32 v105, 6, v113
	s_nop 0
	v_cndmask_b32_e32 v55, v96, v55, vcc
	v_cmp_le_u32_e32 vcc, v105, v98
	v_add_u32_e32 v105, 7, v113
	s_nop 0
	v_cndmask_b32_e32 v56, v96, v56, vcc
	v_cmp_le_u32_e32 vcc, v105, v98
	v_add_u32_e32 v105, 8, v113
	s_nop 0
	v_cndmask_b32_e32 v57, v96, v57, vcc
	v_max3_f32 v105, v50, v51, v52
	v_max3_f32 v106, v53, v54, v55
	v_max3_f32 v105, v105, v56, v57
	v_max_f32_e32 v105, v105, v106
	v_mov_b32_e32 v106, v105
	s_nop 1
	v_permlane32_swap_b32_e32 v105, v106
	v_max_f32_e32 v105, v105, v106
	v_sub_f32_e32 v106, v105, v104
	v_cmp_lt_f32_e32 vcc, s19, v106
	s_mov_b64 s[14:15], vcc
	s_cbranch_vccz .Lat_sp_nors
	v_cndmask_b32_e64 v105, v104, v105, s[14:15]
	v_sub_f32_e32 v104, v104, v105
	v_exp_f32_e32 v104, v104
	s_nop 0
	v_pk_mul_f32 v[32:33], v[104:105], v[32:33] op_sel_hi:[0,1]
	v_pk_mul_f32 v[30:31], v[104:105], v[30:31] op_sel_hi:[0,1]
	v_pk_mul_f32 v[28:29], v[104:105], v[28:29] op_sel_hi:[0,1]
	v_pk_mul_f32 v[26:27], v[104:105], v[26:27] op_sel_hi:[0,1]
	v_pk_mul_f32 v[24:25], v[104:105], v[24:25] op_sel_hi:[0,1]
	v_pk_mul_f32 v[22:23], v[104:105], v[22:23] op_sel_hi:[0,1]
	v_pk_mul_f32 v[20:21], v[104:105], v[20:21] op_sel_hi:[0,1]
	v_pk_mul_f32 v[18:19], v[104:105], v[18:19] op_sel_hi:[0,1]
	v_pk_mul_f32 v[16:17], v[104:105], v[16:17] op_sel_hi:[0,1]
	v_pk_mul_f32 v[14:15], v[104:105], v[14:15] op_sel_hi:[0,1]
	v_pk_mul_f32 v[12:13], v[104:105], v[12:13] op_sel_hi:[0,1]
	v_pk_mul_f32 v[10:11], v[104:105], v[10:11] op_sel_hi:[0,1]
	v_pk_mul_f32 v[8:9], v[104:105], v[8:9] op_sel_hi:[0,1]
	v_pk_mul_f32 v[6:7], v[104:105], v[6:7] op_sel_hi:[0,1]
	v_pk_mul_f32 v[4:5], v[104:105], v[4:5] op_sel_hi:[0,1]
	v_pk_mul_f32 v[2:3], v[104:105], v[2:3] op_sel_hi:[0,1]
	v_mul_f32_e32 v1, v1, v104
	v_mov_b32_e32 v104, v105
	s_mov_b32 s31, 1
.Lat_sp_nors:
	s_cmp_eq_u32 s31, 0
	s_cbranch_scc1 .Lat_sp_nosub
	v_sub_f32_e32 v50, v50, v104
	v_sub_f32_e32 v51, v51, v104
	v_sub_f32_e32 v52, v52, v104
	v_sub_f32_e32 v53, v53, v104
	v_sub_f32_e32 v54, v54, v104
	v_sub_f32_e32 v55, v55, v104
	v_sub_f32_e32 v56, v56, v104
	v_sub_f32_e32 v57, v57, v104
.Lat_sp_nosub:
	v_exp_f32_e32 v105, v50
	v_exp_f32_e32 v106, v51
	v_exp_f32_e32 v107, v52
	v_exp_f32_e32 v108, v53
	v_exp_f32_e32 v109, v54
	v_exp_f32_e32 v110, v55
	v_exp_f32_e32 v111, v56
	v_exp_f32_e32 v112, v57
	v_cvt_pkrtz_f16_f32 v58, v105, v106
	v_cvt_pkrtz_f16_f32 v59, v107, v108
	v_cvt_pkrtz_f16_f32 v60, v109, v110
	v_cvt_pkrtz_f16_f32 v61, v111, v112
	v_pk_add_f16 v62, v58, v59
	v_pk_add_f16 v63, v60, v61
	s_waitcnt lgkmcnt(0)
	v_mfma_f32_32x32x16_f16 v[18:33], v[34:37], v[58:61], v[18:33]
	v_mfma_f32_32x32x16_f16 v[2:17], v[38:41], v[58:61], v[2:17]
	v_pk_add_f16 v62, v62, v63
	v_cvt_f32_f16_e32 v63, v62
	v_cvt_f32_f16_sdwa v62, v62 dst_sel:DWORD dst_unused:UNUSED_PAD src0_sel:WORD_1
	v_add_f32_e32 v62, v62, v63
	v_add_f32_e32 v1, v1, v62
	s_nop 7
	s_branch .Lat_exit

	.amdhsa_kernel _Z14attn_bh_kernelPKDF16_S0_S0_PDF16_i
		.amdhsa_group_segment_fixed_size 0
		.amdhsa_private_segment_fixed_size 0
		.amdhsa_kernarg_size 36
		.amdhsa_user_sgpr_count 2
		.amdhsa_user_sgpr_dispatch_ptr 0
		.amdhsa_user_sgpr_queue_ptr 0
		.amdhsa_user_sgpr_kernarg_segment_ptr 1
		.amdhsa_user_sgpr_dispatch_id 0
		.amdhsa_user_sgpr_kernarg_preload_length 0
		.amdhsa_user_sgpr_kernarg_preload_offset 0
		.amdhsa_user_sgpr_private_segment_size 0
		.amdhsa_uses_dynamic_stack 0
		.amdhsa_enable_private_segment 0
		.amdhsa_system_sgpr_workgroup_id_x 1
		.amdhsa_system_sgpr_workgroup_id_y 0
		.amdhsa_system_sgpr_workgroup_id_z 0
		.amdhsa_system_sgpr_workgroup_info 0
		.amdhsa_system_vgpr_workitem_id 0
		.amdhsa_next_free_vgpr 120
		.amdhsa_next_free_sgpr 32
		.amdhsa_accum_offset 120
		.amdhsa_reserve_vcc 1
		.amdhsa_float_round_mode_32 0
		.amdhsa_float_round_mode_16_64 0
		.amdhsa_float_denorm_mode_32 3
		.amdhsa_float_denorm_mode_16_64 3
		.amdhsa_dx10_clamp 1
		.amdhsa_ieee_mode 1
		.amdhsa_fp16_overflow 0
		.amdhsa_tg_split 0
		.amdhsa_exception_fp_ieee_invalid_op 0
		.amdhsa_exception_fp_denorm_src 0
		.amdhsa_exception_fp_ieee_div_zero 0
		.amdhsa_exception_fp_ieee_overflow 0
		.amdhsa_exception_fp_ieee_underflow 0
		.amdhsa_exception_fp_ieee_inexact 0
		.amdhsa_exception_int_div_zero 0
	.end_amdhsa_kernel

amdhsa.kernels:
  - .agpr_count:     0
    .args:
      - .offset:         0
        .size:           136
        .value_kind:     by_value
      - .actual_access:  read_only
        .address_space:  global
        .offset:         136
        .size:           8
        .value_kind:     global_buffer
      - .actual_access:  read_only
        .address_space:  global
        .offset:         144
        .size:           8
        .value_kind:     global_buffer
      - .actual_access:  read_only
        .address_space:  global
        .offset:         152
        .size:           8
        .value_kind:     global_buffer
      - .actual_access:  read_only
        .address_space:  global
        .offset:         160
        .size:           8
        .value_kind:     global_buffer
      - .actual_access:  write_only
        .address_space:  global
        .offset:         168
        .size:           8
        .value_kind:     global_buffer
      - .actual_access:  write_only
        .address_space:  global
        .offset:         176
        .size:           8
        .value_kind:     global_buffer
    .group_segment_fixed_size: 0
    .kernarg_segment_align: 8
    .kernarg_segment_size: 184
    .language:       OpenCL C
    .language_version:
      - 2
      - 0
    .max_flat_workgroup_size: 256
    .name:           _Z15prologue_kernel8PrepArgsPKfS1_PKiS1_PDF16_Pf
    .private_segment_fixed_size: 0
    .sgpr_count:     36
    .sgpr_spill_count: 0
    .symbol:         _Z15prologue_kernel8PrepArgsPKfS1_PKiS1_PDF16_Pf.kd
    .uniform_work_group_size: 1
    .uses_dynamic_stack: false
    .vgpr_count:     44
    .vgpr_spill_count: 0
    .wavefront_size: 64
  - .agpr_count:     0
    .args:
      - .actual_access:  read_only
        .address_space:  global
        .offset:         0
        .size:           8
        .value_kind:     global_buffer
      - .offset:         8
        .size:           4
        .value_kind:     by_value
      - .offset:         12
        .size:           4
        .value_kind:     by_value
      - .actual_access:  read_only
        .address_space:  global
        .offset:         16
        .size:           8
        .value_kind:     global_buffer
      - .actual_access:  read_only
        .address_space:  global
        .offset:         24
        .size:           8
        .value_kind:     global_buffer
      - .actual_access:  read_only
        .address_space:  global
        .offset:         32
        .size:           8
        .value_kind:     global_buffer
      - .actual_access:  read_only
        .address_space:  global
        .offset:         40
        .size:           8
        .value_kind:     global_buffer
      - .address_space:  global
        .offset:         48
        .size:           8
        .value_kind:     global_buffer
      - .actual_access:  write_only
        .address_space:  global
        .offset:         56
        .size:           8
        .value_kind:     global_buffer
    .group_segment_fixed_size: 0
    .kernarg_segment_align: 8
    .kernarg_segment_size: 64
    .language:       OpenCL C
    .language_version:
      - 2
      - 0
    .max_flat_workgroup_size: 256
    .name:           _Z18ffn2_finish_kernelPKfiiS0_PK15HIP_vector_typeIfLj2EES0_S0_PDF16_PS2_
    .private_segment_fixed_size: 0
    .sgpr_count:     20
    .sgpr_spill_count: 0
    .symbol:         _Z18ffn2_finish_kernelPKfiiS0_PK15HIP_vector_typeIfLj2EES0_S0_PDF16_PS2_.kd
    .uniform_work_group_size: 1
    .uses_dynamic_stack: false
    .vgpr_count:     52
    .vgpr_spill_count: 0
    .wavefront_size: 64
  - .agpr_count:     0
    .args:
      - .actual_access:  read_only
        .address_space:  global
        .offset:         0
        .size:           8
        .value_kind:     global_buffer
      - .actual_access:  read_only
        .address_space:  global
        .offset:         8
        .size:           8
        .value_kind:     global_buffer
      - .actual_access:  read_only
        .address_space:  global
        .offset:         16
        .size:           8
        .value_kind:     global_buffer
      - .actual_access:  write_only
        .address_space:  global
        .offset:         24
        .size:           8
        .value_kind:     global_buffer
      - .offset:         32
        .size:           4
        .value_kind:     by_value
    .group_segment_fixed_size: 0
    .kernarg_segment_align: 8
    .kernarg_segment_size: 36
    .language:       OpenCL C
    .language_version:
      - 2
      - 0
    .max_flat_workgroup_size: 1024
    .name:           _Z14attn_bh_kernelPKDF16_S0_S0_PDF16_i
    .private_segment_fixed_size: 0
    .sgpr_count:     38
    .sgpr_spill_count: 0
    .symbol:         _Z14attn_bh_kernelPKDF16_S0_S0_PDF16_i.kd
    .uniform_work_group_size: 1
    .uses_dynamic_stack: false
    .vgpr_count:     120
    .vgpr_spill_count: 0
    .wavefront_size: 64
  - .agpr_count:     0
    .args:
      - .offset:         0
        .size:           336
        .value_kind:     by_value
    .group_segment_fixed_size: 0
    .kernarg_segment_align: 8
    .kernarg_segment_size: 336
    .language:       OpenCL C
    .language_version:
      - 2
      - 0
    .max_flat_workgroup_size: 256
    .name:           _Z11gemm_kernelILi0EEv8GemmArgs
    .private_segment_fixed_size: 0
    .sgpr_count:     47
    .sgpr_spill_count: 0
    .symbol:         _Z11gemm_kernelILi0EEv8GemmArgs.kd
    .uniform_work_group_size: 1
    .uses_dynamic_stack: false
    .vgpr_count:     198
    .vgpr_spill_count: 0
    .wavefront_size: 64
  - .agpr_count:     0
    .args:
      - .offset:         0
        .size:           336
        .value_kind:     by_value
    .group_segment_fixed_size: 0
    .kernarg_segment_align: 8
    .kernarg_segment_size: 336
    .language:       OpenCL C
    .language_version:
      - 2
      - 0
    .max_flat_workgroup_size: 256
    .name:           _Z11gemm_kernelILi1EEv8GemmArgs
    .private_segment_fixed_size: 0
    .sgpr_count:     43
    .sgpr_spill_count: 0
    .symbol:         _Z11gemm_kernelILi1EEv8GemmArgs.kd
    .uniform_work_group_size: 1
    .uses_dynamic_stack: false
    .vgpr_count:     202
    .vgpr_spill_count: 0
    .wavefront_size: 64
  - .agpr_count:     0
    .args:
      - .offset:         0
        .size:           336
        .value_kind:     by_value
    .group_segment_fixed_size: 0
    .kernarg_segment_align: 8
    .kernarg_segment_size: 336
    .language:       OpenCL C
    .language_version:
      - 2
      - 0
    .max_flat_workgroup_size: 256
    .name:           _Z11gemm_kernelILi2EEv8GemmArgs
    .private_segment_fixed_size: 0
    .sgpr_count:     41
    .sgpr_spill_count: 0
    .symbol:         _Z11gemm_kernelILi2EEv8GemmArgs.kd
    .uniform_work_group_size: 1
    .uses_dynamic_stack: false
    .vgpr_count:     198
    .vgpr_spill_count: 0
    .wavefront_size: 64
  - .agpr_count:     0
    .args:
      - .offset:         0
        .size:           336
        .value_kind:     by_value
      - .offset:         336
        .size:           4
        .value_kind:     hidden_block_count_x
      - .offset:         340
        .size:           4
        .value_kind:     hidden_block_count_y
      - .offset:         344
        .size:           4
        .value_kind:     hidden_block_count_z
      - .offset:         348
        .size:           2
        .value_kind:     hidden_group_size_x
      - .offset:         350
        .size:           2
        .value_kind:     hidden_group_size_y
      - .offset:         352
        .size:           2
        .value_kind:     hidden_group_size_z
      - .offset:         354
        .size:           2
        .value_kind:     hidden_remainder_x
      - .offset:         356
        .size:           2
        .value_kind:     hidden_remainder_y
      - .offset:         358
        .size:           2
        .value_kind:     hidden_remainder_z
      - .offset:         376
        .size:           8
        .value_kind:     hidden_global_offset_x
      - .offset:         384
        .size:           8
        .value_kind:     hidden_global_offset_y
      - .offset:         392
        .size:           8
        .value_kind:     hidden_global_offset_z
      - .offset:         400
        .size:           2
        .value_kind:     hidden_grid_dims
      - .offset:         456
        .size:           4
        .value_kind:     hidden_dynamic_lds_size
    .group_segment_fixed_size: 0
    .kernarg_segment_align: 8
    .kernarg_segment_size: 592
    .language:       OpenCL C
    .language_version:
      - 2
      - 0
    .max_flat_workgroup_size: 512
    .name:           _Z14gemm256_kernelILi0ELi512ELi1536EEv8GemmArgs
    .private_segment_fixed_size: 0
    .sgpr_count:     78
    .sgpr_spill_count: 0
    .symbol:         _Z14gemm256_kernelILi0ELi512ELi1536EEv8GemmArgs.kd
    .uniform_work_group_size: 1
    .uses_dynamic_stack: false
    .vgpr_count:     256
    .vgpr_spill_count: 0
    .wavefront_size: 64
  - .agpr_count:     0
    .args:
      - .offset:         0
        .size:           336
        .value_kind:     by_value
      - .offset:         336
        .size:           4
        .value_kind:     hidden_block_count_x
      - .offset:         340
        .size:           4
        .value_kind:     hidden_block_count_y
      - .offset:         344
        .size:           4
        .value_kind:     hidden_block_count_z
      - .offset:         348
        .size:           2
        .value_kind:     hidden_group_size_x
      - .offset:         350
        .size:           2
        .value_kind:     hidden_group_size_y
      - .offset:         352
        .size:           2
        .value_kind:     hidden_group_size_z
      - .offset:         354
        .size:           2
        .value_kind:     hidden_remainder_x
      - .offset:         356
        .size:           2
        .value_kind:     hidden_remainder_y
      - .offset:         358
        .size:           2
        .value_kind:     hidden_remainder_z
      - .offset:         376
        .size:           8
        .value_kind:     hidden_global_offset_x
      - .offset:         384
        .size:           8
        .value_kind:     hidden_global_offset_y
      - .offset:         392
        .size:           8
        .value_kind:     hidden_global_offset_z
      - .offset:         400
        .size:           2
        .value_kind:     hidden_grid_dims
      - .offset:         456
        .size:           4
        .value_kind:     hidden_dynamic_lds_size
    .group_segment_fixed_size: 0
    .kernarg_segment_align: 8
    .kernarg_segment_size: 592
    .language:       OpenCL C
    .language_version:
      - 2
      - 0
    .max_flat_workgroup_size: 512
    .name:           _Z14gemm256_kernelILi0ELi512ELi1024EEv8GemmArgs
    .private_segment_fixed_size: 0
    .sgpr_count:     78
    .sgpr_spill_count: 0
    .symbol:         _Z14gemm256_kernelILi0ELi512ELi1024EEv8GemmArgs.kd
    .uniform_work_group_size: 1
    .uses_dynamic_stack: false
    .vgpr_count:     256
    .vgpr_spill_count: 0
    .wavefront_size: 64
  - .agpr_count:     0
    .args:
      - .offset:         0
        .size:           336
        .value_kind:     by_value
      - .offset:         336
        .size:           4
        .value_kind:     hidden_block_count_x
      - .offset:         340
        .size:           4
        .value_kind:     hidden_block_count_y
      - .offset:         344
        .size:           4
        .value_kind:     hidden_block_count_z
      - .offset:         348
        .size:           2
        .value_kind:     hidden_group_size_x
      - .offset:         350
        .size:           2
        .value_kind:     hidden_group_size_y
      - .offset:         352
        .size:           2
        .value_kind:     hidden_group_size_z
      - .offset:         354
        .size:           2
        .value_kind:     hidden_remainder_x
      - .offset:         356
        .size:           2
        .value_kind:     hidden_remainder_y
      - .offset:         358
        .size:           2
        .value_kind:     hidden_remainder_z
      - .offset:         376
        .size:           8
        .value_kind:     hidden_global_offset_x
      - .offset:         384
        .size:           8
        .value_kind:     hidden_global_offset_y
      - .offset:         392
        .size:           8
        .value_kind:     hidden_global_offset_z
      - .offset:         400
        .size:           2
        .value_kind:     hidden_grid_dims
      - .offset:         456
        .size:           4
        .value_kind:     hidden_dynamic_lds_size
    .group_segment_fixed_size: 0
    .kernarg_segment_align: 8
    .kernarg_segment_size: 592
    .language:       OpenCL C
    .language_version:
      - 2
      - 0
    .max_flat_workgroup_size: 512
    .name:           _Z14gemm256_kernelILi1ELi512ELi512EEv8GemmArgs
    .private_segment_fixed_size: 0
    .sgpr_count:     81
    .sgpr_spill_count: 0
    .symbol:         _Z14gemm256_kernelILi1ELi512ELi512EEv8GemmArgs.kd
    .uniform_work_group_size: 1
    .uses_dynamic_stack: false
    .vgpr_count:     256
    .vgpr_spill_count: 0
    .wavefront_size: 64
  - .agpr_count:     0
    .args:
      - .offset:         0
        .size:           336
        .value_kind:     by_value
      - .offset:         336
        .size:           4
        .value_kind:     hidden_block_count_x
      - .offset:         340
        .size:           4
        .value_kind:     hidden_block_count_y
      - .offset:         344
        .size:           4
        .value_kind:     hidden_block_count_z
      - .offset:         348
        .size:           2
        .value_kind:     hidden_group_size_x
      - .offset:         350
        .size:           2
        .value_kind:     hidden_group_size_y
      - .offset:         352
        .size:           2
        .value_kind:     hidden_group_size_z
      - .offset:         354
        .size:           2
        .value_kind:     hidden_remainder_x
      - .offset:         356
        .size:           2
        .value_kind:     hidden_remainder_y
      - .offset:         358
        .size:           2
        .value_kind:     hidden_remainder_z
      - .offset:         376
        .size:           8
        .value_kind:     hidden_global_offset_x
      - .offset:         384
        .size:           8
        .value_kind:     hidden_global_offset_y
      - .offset:         392
        .size:           8
        .value_kind:     hidden_global_offset_z
      - .offset:         400
        .size:           2
        .value_kind:     hidden_grid_dims
      - .offset:         456
        .size:           4
        .value_kind:     hidden_dynamic_lds_size
    .group_segment_fixed_size: 0
    .kernarg_segment_align: 8
    .kernarg_segment_size: 592
    .language:       OpenCL C
    .language_version:
      - 2
      - 0
    .max_flat_workgroup_size: 512
    .name:           _Z14gemm256_kernelILi2ELi512ELi2048EEv8GemmArgs
    .private_segment_fixed_size: 0
    .sgpr_count:     68
    .sgpr_spill_count: 0
    .symbol:         _Z14gemm256_kernelILi2ELi512ELi2048EEv8GemmArgs.kd
    .uniform_work_group_size: 1
    .uses_dynamic_stack: false
    .vgpr_count:     254
    .vgpr_spill_count: 0
    .wavefront_size: 64
  - .agpr_count:     0
    .args:
      - .offset:         0
        .size:           336
        .value_kind:     by_value
      - .offset:         336
        .size:           4
        .value_kind:     hidden_block_count_x
      - .offset:         340
        .size:           4
        .value_kind:     hidden_block_count_y
      - .offset:         344
        .size:           4
        .value_kind:     hidden_block_count_z
      - .offset:         348
        .size:           2
        .value_kind:     hidden_group_size_x
      - .offset:         350
        .size:           2
        .value_kind:     hidden_group_size_y
      - .offset:         352
        .size:           2
        .value_kind:     hidden_group_size_z
      - .offset:         354
        .size:           2
        .value_kind:     hidden_remainder_x
      - .offset:         356
        .size:           2
        .value_kind:     hidden_remainder_y
      - .offset:         358
        .size:           2
        .value_kind:     hidden_remainder_z
      - .offset:         376
        .size:           8
        .value_kind:     hidden_global_offset_x
      - .offset:         384
        .size:           8
        .value_kind:     hidden_global_offset_y
      - .offset:         392
        .size:           8
        .value_kind:     hidden_global_offset_z
      - .offset:         400
        .size:           2
        .value_kind:     hidden_grid_dims
      - .offset:         456
        .size:           4
        .value_kind:     hidden_dynamic_lds_size
    .group_segment_fixed_size: 0
    .kernarg_segment_align: 8
    .kernarg_segment_size: 592
    .language:       OpenCL C
    .language_version:
      - 2
      - 0
    .max_flat_workgroup_size: 512
    .name:           _Z14gemm256_kernelILi1ELi2048ELi512EEv8GemmArgs
    .private_segment_fixed_size: 0
    .sgpr_count:     76
    .sgpr_spill_count: 0
    .symbol:         _Z14gemm256_kernelILi1ELi2048ELi512EEv8GemmArgs.kd
    .uniform_work_group_size: 1
    .uses_dynamic_stack: false
    .vgpr_count:     256
    .vgpr_spill_count: 0
    .wavefront_size: 64
  - .agpr_count:     0
    .args:
      - .offset:         0
        .size:           336
        .value_kind:     by_value
    .group_segment_fixed_size: 0
    .kernarg_segment_align: 8
    .kernarg_segment_size: 336
    .language:       OpenCL C
    .language_version:
      - 2
      - 0
    .max_flat_workgroup_size: 256
    .name:           _Z11gemm_kernelILi4EEv8GemmArgs
    .private_segment_fixed_size: 0
    .sgpr_count:     42
    .sgpr_spill_count: 0
    .symbol:         _Z11gemm_kernelILi4EEv8GemmArgs.kd
    .uniform_work_group_size: 1
    .uses_dynamic_stack: false
    .vgpr_count:     196
    .vgpr_spill_count: 0
    .wavefront_size: 64
  - .agpr_count:     0
    .args:
      - .offset:         0
        .size:           336
        .value_kind:     by_value
    .group_segment_fixed_size: 0
    .kernarg_segment_align: 8
    .kernarg_segment_size: 336
    .language:       OpenCL C
    .language_version:
      - 2
      - 0
    .max_flat_workgroup_size: 256
    .name:           _Z11gemm_kernelILi3EEv8GemmArgs
    .private_segment_fixed_size: 0
    .sgpr_count:     38
    .sgpr_spill_count: 0
    .symbol:         _Z11gemm_kernelILi3EEv8GemmArgs.kd
    .uniform_work_group_size: 1
    .uses_dynamic_stack: false
    .vgpr_count:     200
    .vgpr_spill_count: 0
    .wavefront_size: 64
